# rot1: pf1 + IN epilogue Q/K tiles: rotary table rows of m=2,3 requested together with m=0,1 (one table round trip per 128-row half instead of two)
# baseline (speedup 1.0000x reference)
; #define EFENCE() asm volatile("" ::: "memory")
;     __device__ __forceinline__ bool operator()(f32x4 (&acc)[2][2][4][2], const pg8::Unit& u, int wr, int wc, int fr, int fq) const {
;     ...
;         if (pn < 8) {
;             bf16_t* dst = pn < 4 ? Q : Kb; const float sc = pn < 4 ? QSCALE : 1.0f; const int colb = (pn & 3) * 256 + wc * 32 + 8 * fq;
;             const bool rot = ((wc & 1) == 0) && (fq < 2);
; #pragma unroll
;             for (int ai = 0; ai < 2; ++ai)
; #pragma unroll
;               for (int mh = 0; mh < 2; ++mh) {
;                 f32x4 c4[2], s4[2];
; #pragma unroll
;                 for (int q = 0; q < 2; ++q) { c4[q] = (f32x4){1.f, 1.f, 1.f, 1.f}; s4[q] = (f32x4){0.f, 0.f, 0.f, 0.f};
;                     if (rot) { const int t = (row0 + ai * 128 + (2 * mh + q) * 16) & (SEQ - 1); c4[q] = *(const f32x4*)(cosT + t * 8 + 4 * fq); s4[q] = *(const f32x4*)(sinT + t * 8 + 4 * fq); } }
; #pragma unroll
;                 for (int q = 0; q < 2; ++q) { const int m = 2 * mh + q; const int row = row0 + ai * 128 + m * 16; const float rsv = RS_AT(ai, m);
; #pragma unroll
;                     for (int bj = 0; bj < 2; ++bj) { f32x4 x1 = acc[ai][bj][m][0] * rsv, x2 = acc[ai][bj][m][1] * rsv;
;                         const f32x4 y1 = x1 * c4[q] - x2 * s4[q], y2 = x2 * c4[q] + x1 * s4[q];
;                         if (rot) { x1 = y1; x2 = y2; }
;                         st8(dst + (size_t)row * DM + colb + bj * 128, x1 * sc, x2 * sc); } }
;                 EFENCE(); }
.LBB0_739:
	s_or_b64 exec, exec, s[4:5]
	v_mov_b32_e32 v220, 1.0
	v_mov_b32_e32 v221, 1.0
	v_mov_b32_e32 v222, 1.0
	v_mov_b32_e32 v223, 1.0
	v_mov_b32_e32 v224, 0
	v_mov_b32_e32 v225, 0
	v_mov_b32_e32 v226, 0
	v_mov_b32_e32 v227, 0
	v_mov_b32_e32 v228, 1.0
	v_mov_b32_e32 v229, 1.0
	v_mov_b32_e32 v230, 1.0
	v_mov_b32_e32 v231, 1.0
	v_mov_b32_e32 v232, 0
	v_mov_b32_e32 v233, 0
	v_mov_b32_e32 v234, 0
	v_mov_b32_e32 v235, 0
	s_and_saveexec_b64 s[4:5], s[0:1]
	s_cbranch_execz .Lrot_741
	v_and_b32_e32 v160, 0xf9e0, v147
	v_lshl_add_u64 v[218:219], v[168:169], 0, v[160:161]
	global_load_dwordx4 v[220:223], v[218:219], off offset:1024
	global_load_dwordx4 v[228:231], v[218:219], off offset:1536
	v_lshl_add_u64 v[218:219], v[170:171], 0, v[160:161]
	global_load_dwordx4 v[224:227], v[218:219], off offset:1024
	global_load_dwordx4 v[232:235], v[218:219], off offset:1536
.Lrot_741:
	s_or_b64 exec, exec, s[4:5]
	s_cmp_lt_i32 s29, 4
	s_cselect_b64 vcc, -1, 0
	s_and_b64 s[2:3], vcc, exec
	v_readlane_b32 s2, v252, 16
	v_readlane_b32 s3, v252, 17
	v_readlane_b32 s4, v251, 43
	s_cselect_b32 s3, s3, s4
	v_readlane_b32 s4, v251, 42
	s_cselect_b32 s2, s2, s4
	s_lshl_b32 s4, s29, 8
	v_pk_mul_f32 v[122:123], v[122:123], v[198:199] op_sel_hi:[1,0]
	v_pk_mul_f32 v[120:121], v[120:121], v[198:199] op_sel_hi:[1,0]
	v_mov_b32_e32 v129, 0x3e38aa3b
	s_and_b32 s4, s4, 0x300
	v_pk_mul_f32 v[126:127], v[126:127], v[198:199] op_sel_hi:[1,0]
	v_pk_mul_f32 v[124:125], v[124:125], v[198:199] op_sel_hi:[1,0]
	s_waitcnt vmcnt(5)
	v_pk_mul_f32 v[192:193], v[122:123], v[140:141]
	v_pk_mul_f32 v[208:209], v[120:121], v[138:139]
	v_cndmask_b32_e32 v204, 1.0, v129, vcc
	v_or_b32_e32 v129, s4, v203
	s_waitcnt vmcnt(0)
	v_pk_fma_f32 v[192:193], v[126:127], v[144:145], v[192:193]
	v_pk_fma_f32 v[208:209], v[124:125], v[142:143], v[208:209]
	v_pk_mul_f32 v[210:211], v[122:123], v[144:145]
	v_pk_mul_f32 v[216:217], v[120:121], v[142:143]
	v_lshlrev_b32_e32 v160, 1, v129
	v_pk_fma_f32 v[210:211], v[126:127], v[140:141], v[210:211] neg_lo:[0,0,1] neg_hi:[0,0,1]
	v_pk_fma_f32 v[216:217], v[124:125], v[138:139], v[216:217] neg_lo:[0,0,1] neg_hi:[0,0,1]
	v_cndmask_b32_e64 v123, v123, v193, s[0:1]
	v_cndmask_b32_e64 v122, v122, v192, s[0:1]
	v_cndmask_b32_e64 v121, v121, v209, s[0:1]
	v_cndmask_b32_e64 v120, v120, v208, s[0:1]
	v_lshl_add_u64 v[206:207], s[2:3], 0, v[160:161]
	v_lshlrev_b64 v[190:191], 11, v[184:185]
	v_cndmask_b32_e64 v127, v127, v211, s[0:1]
	v_cndmask_b32_e64 v126, v126, v210, s[0:1]
	v_cndmask_b32_e64 v125, v125, v217, s[0:1]
	v_cndmask_b32_e64 v124, v124, v216, s[0:1]
	v_pk_mul_f32 v[192:193], v[204:205], v[122:123] op_sel_hi:[0,1]
	v_pk_mul_f32 v[122:123], v[204:205], v[120:121] op_sel_hi:[0,1]
	v_lshl_add_u64 v[190:191], v[206:207], 0, v[190:191]
	v_pk_mul_f32 v[126:127], v[204:205], v[126:127] op_sel_hi:[0,1]
	v_pk_mul_f32 v[124:125], v[204:205], v[124:125] op_sel_hi:[0,1]
	v_cvt_pk_bf16_f32 v120, v124, v125
	v_cvt_pk_bf16_f32 v121, v126, v127
	v_cvt_pk_bf16_f32 v122, v122, v123
	v_cvt_pk_bf16_f32 v123, v192, v193
	v_pk_mul_f32 v[114:115], v[114:115], v[198:199] op_sel_hi:[1,0]
	v_pk_mul_f32 v[112:113], v[112:113], v[198:199] op_sel_hi:[1,0]
	global_store_dwordx4 v[190:191], v[120:123], off
	v_pk_mul_f32 v[118:119], v[118:119], v[198:199] op_sel_hi:[1,0]
	v_pk_mul_f32 v[116:117], v[116:117], v[198:199] op_sel_hi:[1,0]
	v_pk_mul_f32 v[120:121], v[114:115], v[140:141]
	v_pk_mul_f32 v[122:123], v[112:113], v[138:139]
	v_pk_fma_f32 v[120:121], v[118:119], v[144:145], v[120:121]
	v_pk_fma_f32 v[122:123], v[116:117], v[142:143], v[122:123]
	v_pk_mul_f32 v[124:125], v[114:115], v[144:145]
	v_pk_mul_f32 v[126:127], v[112:113], v[142:143]
	v_pk_fma_f32 v[124:125], v[118:119], v[140:141], v[124:125] neg_lo:[0,0,1] neg_hi:[0,0,1]
	v_pk_fma_f32 v[126:127], v[116:117], v[138:139], v[126:127] neg_lo:[0,0,1] neg_hi:[0,0,1]
	v_cndmask_b32_e64 v115, v115, v121, s[0:1]
	v_cndmask_b32_e64 v114, v114, v120, s[0:1]
	v_cndmask_b32_e64 v113, v113, v123, s[0:1]
	v_cndmask_b32_e64 v112, v112, v122, s[0:1]
	v_cndmask_b32_e64 v119, v119, v125, s[0:1]
	v_cndmask_b32_e64 v118, v118, v124, s[0:1]
	v_cndmask_b32_e64 v117, v117, v127, s[0:1]
	v_cndmask_b32_e64 v116, v116, v126, s[0:1]
	v_pk_mul_f32 v[120:121], v[204:205], v[114:115] op_sel_hi:[0,1]
	v_pk_mul_f32 v[114:115], v[204:205], v[112:113] op_sel_hi:[0,1]
	v_pk_mul_f32 v[118:119], v[204:205], v[118:119] op_sel_hi:[0,1]
	v_pk_mul_f32 v[116:117], v[204:205], v[116:117] op_sel_hi:[0,1]
	v_cvt_pk_bf16_f32 v112, v116, v117
	v_cvt_pk_bf16_f32 v113, v118, v119
	v_cvt_pk_bf16_f32 v114, v114, v115
	v_cvt_pk_bf16_f32 v115, v120, v121
	v_pk_mul_f32 v[106:107], v[106:107], v[154:155] op_sel_hi:[1,0]
	v_pk_mul_f32 v[104:105], v[104:105], v[154:155] op_sel_hi:[1,0]
	global_store_dwordx4 v[190:191], v[112:115], off offset:256
	v_pk_mul_f32 v[110:111], v[110:111], v[154:155] op_sel_hi:[1,0]
	v_pk_mul_f32 v[108:109], v[108:109], v[154:155] op_sel_hi:[1,0]
	v_pk_mul_f32 v[114:115], v[104:105], v[130:131]
	v_pk_mul_f32 v[116:117], v[106:107], v[132:133]
	v_pk_fma_f32 v[114:115], v[108:109], v[134:135], v[114:115]
	v_pk_fma_f32 v[116:117], v[110:111], v[136:137], v[116:117]
	v_pk_mul_f32 v[118:119], v[104:105], v[134:135]
	v_pk_mul_f32 v[120:121], v[106:107], v[136:137]
	v_pk_fma_f32 v[118:119], v[108:109], v[130:131], v[118:119] neg_lo:[0,0,1] neg_hi:[0,0,1]
	v_pk_fma_f32 v[120:121], v[110:111], v[132:133], v[120:121] neg_lo:[0,0,1] neg_hi:[0,0,1]
	v_cndmask_b32_e64 v107, v107, v117, s[0:1]
	v_cndmask_b32_e64 v106, v106, v116, s[0:1]
	v_cndmask_b32_e64 v105, v105, v115, s[0:1]
	v_cndmask_b32_e64 v104, v104, v114, s[0:1]
	v_lshlrev_b64 v[112:113], 11, v[196:197]
; #define EFENCE() asm volatile("" ::: "memory")
;     __device__ __forceinline__ bool operator()(f32x4 (&acc)[2][2][4][2], const pg8::Unit& u, int wr, int wc, int fr, int fq) const {
;     ...
;                 for (int q = 0; q < 2; ++q) { c4[q] = (f32x4){1.f, 1.f, 1.f, 1.f}; s4[q] = (f32x4){0.f, 0.f, 0.f, 0.f};
;                     if (rot) { const int t = (row0 + ai * 128 + (2 * mh + q) * 16) & (SEQ - 1); c4[q] = *(const f32x4*)(cosT + t * 8 + 4 * fq); s4[q] = *(const f32x4*)(sinT + t * 8 + 4 * fq); } }
; #pragma unroll
;                 for (int q = 0; q < 2; ++q) { const int m = 2 * mh + q; const int row = row0 + ai * 128 + m * 16; const float rsv = RS_AT(ai, m);
; #pragma unroll
;                     for (int bj = 0; bj < 2; ++bj) { f32x4 x1 = acc[ai][bj][m][0] * rsv, x2 = acc[ai][bj][m][1] * rsv;
;                         const f32x4 y1 = x1 * c4[q] - x2 * s4[q], y2 = x2 * c4[q] + x1 * s4[q];
;                         if (rot) { x1 = y1; x2 = y2; }
;                         st8(dst + (size_t)row * DM + colb + bj * 128, x1 * sc, x2 * sc); } }
;                 EFENCE(); }
	v_cndmask_b32_e64 v111, v111, v121, s[0:1]
	v_cndmask_b32_e64 v110, v110, v120, s[0:1]
	v_cndmask_b32_e64 v109, v109, v119, s[0:1]
	v_cndmask_b32_e64 v108, v108, v118, s[0:1]
	v_pk_mul_f32 v[114:115], v[204:205], v[106:107] op_sel_hi:[0,1]
	v_pk_mul_f32 v[106:107], v[204:205], v[104:105] op_sel_hi:[0,1]
	v_lshl_add_u64 v[112:113], v[206:207], 0, v[112:113]
	v_pk_mul_f32 v[110:111], v[204:205], v[110:111] op_sel_hi:[0,1]
	v_pk_mul_f32 v[108:109], v[204:205], v[108:109] op_sel_hi:[0,1]
	v_cvt_pk_bf16_f32 v104, v108, v109
	v_cvt_pk_bf16_f32 v105, v110, v111
	v_cvt_pk_bf16_f32 v106, v106, v107
	v_cvt_pk_bf16_f32 v107, v114, v115
	v_pk_mul_f32 v[98:99], v[98:99], v[154:155] op_sel_hi:[1,0]
	v_pk_mul_f32 v[96:97], v[96:97], v[154:155] op_sel_hi:[1,0]
	global_store_dwordx4 v[112:113], v[104:107], off
	v_pk_mul_f32 v[102:103], v[102:103], v[154:155] op_sel_hi:[1,0]
	v_pk_mul_f32 v[100:101], v[100:101], v[154:155] op_sel_hi:[1,0]
	v_pk_mul_f32 v[104:105], v[96:97], v[130:131]
	v_pk_mul_f32 v[106:107], v[98:99], v[132:133]
	v_pk_fma_f32 v[104:105], v[100:101], v[134:135], v[104:105]
	v_pk_fma_f32 v[106:107], v[102:103], v[136:137], v[106:107]
	v_pk_mul_f32 v[108:109], v[96:97], v[134:135]
	v_pk_mul_f32 v[110:111], v[98:99], v[136:137]
	v_pk_fma_f32 v[108:109], v[100:101], v[130:131], v[108:109] neg_lo:[0,0,1] neg_hi:[0,0,1]
	v_pk_fma_f32 v[110:111], v[102:103], v[132:133], v[110:111] neg_lo:[0,0,1] neg_hi:[0,0,1]
	v_cndmask_b32_e64 v99, v99, v107, s[0:1]
	v_cndmask_b32_e64 v98, v98, v106, s[0:1]
	v_cndmask_b32_e64 v97, v97, v105, s[0:1]
	v_cndmask_b32_e64 v96, v96, v104, s[0:1]
	v_cndmask_b32_e64 v103, v103, v111, s[0:1]
	v_cndmask_b32_e64 v102, v102, v110, s[0:1]
	v_cndmask_b32_e64 v101, v101, v109, s[0:1]
	v_cndmask_b32_e64 v100, v100, v108, s[0:1]
	v_pk_mul_f32 v[104:105], v[204:205], v[98:99] op_sel_hi:[0,1]
	v_pk_mul_f32 v[98:99], v[204:205], v[96:97] op_sel_hi:[0,1]
	v_pk_mul_f32 v[102:103], v[204:205], v[102:103] op_sel_hi:[0,1]
	v_pk_mul_f32 v[100:101], v[204:205], v[100:101] op_sel_hi:[0,1]
	v_cvt_pk_bf16_f32 v96, v100, v101
	v_cvt_pk_bf16_f32 v97, v102, v103
	v_cvt_pk_bf16_f32 v98, v98, v99
	v_cvt_pk_bf16_f32 v99, v104, v105
	global_store_dwordx4 v[112:113], v[96:99], off offset:256
	v_pk_mul_f32 v[90:91], v[90:91], v[202:203] op_sel_hi:[1,0]
	v_pk_mul_f32 v[88:89], v[88:89], v[202:203] op_sel_hi:[1,0]
	v_pk_mul_f32 v[94:95], v[94:95], v[202:203] op_sel_hi:[1,0]
	v_pk_mul_f32 v[92:93], v[92:93], v[202:203] op_sel_hi:[1,0]
	v_pk_mul_f32 v[110:111], v[90:91], v[222:223]
	v_pk_mul_f32 v[112:113], v[88:89], v[220:221]
	v_pk_fma_f32 v[110:111], v[94:95], v[226:227], v[110:111]
	v_pk_fma_f32 v[112:113], v[92:93], v[224:225], v[112:113]
	v_pk_mul_f32 v[114:115], v[90:91], v[226:227]
	v_pk_mul_f32 v[116:117], v[88:89], v[224:225]
	v_mov_b32_e32 v205, v204
	v_pk_fma_f32 v[114:115], v[94:95], v[222:223], v[114:115] neg_lo:[0,0,1] neg_hi:[0,0,1]
	v_pk_fma_f32 v[116:117], v[92:93], v[220:221], v[116:117] neg_lo:[0,0,1] neg_hi:[0,0,1]
	v_cndmask_b32_e64 v91, v91, v111, s[0:1]
	v_cndmask_b32_e64 v90, v90, v110, s[0:1]
	v_cndmask_b32_e64 v89, v89, v113, s[0:1]
	v_cndmask_b32_e64 v88, v88, v112, s[0:1]
	v_mov_b32_e32 v110, v204
	v_mov_b32_e32 v111, v204
	v_lshlrev_b64 v[108:109], 11, v[188:189]
	v_cndmask_b32_e64 v95, v95, v115, s[0:1]
	v_cndmask_b32_e64 v94, v94, v114, s[0:1]
	v_cndmask_b32_e64 v93, v93, v117, s[0:1]
	v_cndmask_b32_e64 v92, v92, v116, s[0:1]
	v_pk_mul_f32 v[112:113], v[110:111], v[90:91]
	v_pk_mul_f32 v[90:91], v[204:205], v[88:89]
	v_lshl_add_u64 v[108:109], v[206:207], 0, v[108:109]
	v_pk_mul_f32 v[94:95], v[110:111], v[94:95]
	v_pk_mul_f32 v[92:93], v[204:205], v[92:93]
	v_pk_mul_f32 v[82:83], v[82:83], v[202:203] op_sel_hi:[1,0]
	v_cvt_pk_bf16_f32 v88, v92, v93
	v_cvt_pk_bf16_f32 v89, v94, v95
	v_cvt_pk_bf16_f32 v90, v90, v91
	v_cvt_pk_bf16_f32 v91, v112, v113
	v_pk_mul_f32 v[80:81], v[80:81], v[202:203] op_sel_hi:[1,0]
	global_store_dwordx4 v[108:109], v[88:91], off
	v_pk_mul_f32 v[86:87], v[86:87], v[202:203] op_sel_hi:[1,0]
	v_pk_mul_f32 v[84:85], v[84:85], v[202:203] op_sel_hi:[1,0]
	v_pk_mul_f32 v[88:89], v[82:83], v[222:223]
	v_pk_mul_f32 v[90:91], v[80:81], v[220:221]
	v_pk_fma_f32 v[88:89], v[86:87], v[226:227], v[88:89]
	v_pk_fma_f32 v[90:91], v[84:85], v[224:225], v[90:91]
	v_pk_mul_f32 v[92:93], v[82:83], v[226:227]
	v_pk_mul_f32 v[94:95], v[80:81], v[224:225]
; #define EFENCE() asm volatile("" ::: "memory")
;     __device__ __forceinline__ bool operator()(f32x4 (&acc)[2][2][4][2], const pg8::Unit& u, int wr, int wc, int fr, int fq) const {
;     ...
;                 for (int q = 0; q < 2; ++q) { c4[q] = (f32x4){1.f, 1.f, 1.f, 1.f}; s4[q] = (f32x4){0.f, 0.f, 0.f, 0.f};
;                     if (rot) { const int t = (row0 + ai * 128 + (2 * mh + q) * 16) & (SEQ - 1); c4[q] = *(const f32x4*)(cosT + t * 8 + 4 * fq); s4[q] = *(const f32x4*)(sinT + t * 8 + 4 * fq); } }
; #pragma unroll
;                 for (int q = 0; q < 2; ++q) { const int m = 2 * mh + q; const int row = row0 + ai * 128 + m * 16; const float rsv = RS_AT(ai, m);
; #pragma unroll
;                     for (int bj = 0; bj < 2; ++bj) { f32x4 x1 = acc[ai][bj][m][0] * rsv, x2 = acc[ai][bj][m][1] * rsv;
;                         const f32x4 y1 = x1 * c4[q] - x2 * s4[q], y2 = x2 * c4[q] + x1 * s4[q];
;                         if (rot) { x1 = y1; x2 = y2; }
;                         st8(dst + (size_t)row * DM + colb + bj * 128, x1 * sc, x2 * sc); } }
;                 EFENCE(); }
	v_pk_fma_f32 v[92:93], v[86:87], v[222:223], v[92:93] neg_lo:[0,0,1] neg_hi:[0,0,1]
	v_pk_fma_f32 v[94:95], v[84:85], v[220:221], v[94:95] neg_lo:[0,0,1] neg_hi:[0,0,1]
	v_cndmask_b32_e64 v83, v83, v89, s[0:1]
	v_cndmask_b32_e64 v82, v82, v88, s[0:1]
	v_cndmask_b32_e64 v81, v81, v91, s[0:1]
	v_cndmask_b32_e64 v80, v80, v90, s[0:1]
	v_cndmask_b32_e64 v87, v87, v93, s[0:1]
	v_cndmask_b32_e64 v86, v86, v92, s[0:1]
	v_cndmask_b32_e64 v85, v85, v95, s[0:1]
	v_cndmask_b32_e64 v84, v84, v94, s[0:1]
	v_pk_mul_f32 v[88:89], v[110:111], v[82:83]
	v_pk_mul_f32 v[82:83], v[204:205], v[80:81]
	v_pk_mul_f32 v[86:87], v[110:111], v[86:87]
	v_pk_mul_f32 v[84:85], v[204:205], v[84:85]
	v_pk_mul_f32 v[74:75], v[74:75], v[200:201] op_sel_hi:[1,0]
	v_cvt_pk_bf16_f32 v80, v84, v85
	v_cvt_pk_bf16_f32 v81, v86, v87
	v_cvt_pk_bf16_f32 v82, v82, v83
	v_cvt_pk_bf16_f32 v83, v88, v89
	v_pk_mul_f32 v[72:73], v[72:73], v[200:201] op_sel_hi:[1,0]
	global_store_dwordx4 v[108:109], v[80:83], off offset:256
	v_pk_mul_f32 v[78:79], v[78:79], v[200:201] op_sel_hi:[1,0]
	v_pk_mul_f32 v[76:77], v[76:77], v[200:201] op_sel_hi:[1,0]
	v_pk_mul_f32 v[82:83], v[72:73], v[228:229]
	v_pk_mul_f32 v[84:85], v[74:75], v[230:231]
	v_pk_fma_f32 v[82:83], v[76:77], v[232:233], v[82:83]
	v_pk_fma_f32 v[84:85], v[78:79], v[234:235], v[84:85]
	v_pk_mul_f32 v[86:87], v[72:73], v[232:233]
	v_pk_mul_f32 v[88:89], v[74:75], v[234:235]
	v_pk_fma_f32 v[86:87], v[76:77], v[228:229], v[86:87] neg_lo:[0,0,1] neg_hi:[0,0,1]
	v_pk_fma_f32 v[88:89], v[78:79], v[230:231], v[88:89] neg_lo:[0,0,1] neg_hi:[0,0,1]
	v_cndmask_b32_e64 v75, v75, v85, s[0:1]
	v_cndmask_b32_e64 v74, v74, v84, s[0:1]
	v_cndmask_b32_e64 v73, v73, v83, s[0:1]
	v_cndmask_b32_e64 v72, v72, v82, s[0:1]
	v_lshlrev_b64 v[80:81], 11, v[186:187]
	v_cndmask_b32_e64 v79, v79, v89, s[0:1]
	v_cndmask_b32_e64 v78, v78, v88, s[0:1]
	v_cndmask_b32_e64 v77, v77, v87, s[0:1]
	v_cndmask_b32_e64 v76, v76, v86, s[0:1]
	v_pk_mul_f32 v[82:83], v[110:111], v[74:75]
	v_pk_mul_f32 v[74:75], v[204:205], v[72:73]
	v_lshl_add_u64 v[80:81], v[206:207], 0, v[80:81]
	v_pk_mul_f32 v[78:79], v[110:111], v[78:79]
	v_pk_mul_f32 v[76:77], v[204:205], v[76:77]
	v_pk_mul_f32 v[66:67], v[66:67], v[200:201] op_sel_hi:[1,0]
	v_cvt_pk_bf16_f32 v72, v76, v77
	v_cvt_pk_bf16_f32 v73, v78, v79
	v_cvt_pk_bf16_f32 v74, v74, v75
	v_cvt_pk_bf16_f32 v75, v82, v83
	v_pk_mul_f32 v[64:65], v[64:65], v[200:201] op_sel_hi:[1,0]
	global_store_dwordx4 v[80:81], v[72:75], off
	v_pk_mul_f32 v[70:71], v[70:71], v[200:201] op_sel_hi:[1,0]
	v_pk_mul_f32 v[68:69], v[68:69], v[200:201] op_sel_hi:[1,0]
	v_pk_mul_f32 v[72:73], v[64:65], v[228:229]
	v_pk_mul_f32 v[74:75], v[66:67], v[230:231]
	v_pk_fma_f32 v[72:73], v[68:69], v[232:233], v[72:73]
	v_pk_fma_f32 v[74:75], v[70:71], v[234:235], v[74:75]
	v_pk_mul_f32 v[76:77], v[64:65], v[232:233]
	v_pk_mul_f32 v[78:79], v[66:67], v[234:235]
	v_pk_fma_f32 v[76:77], v[68:69], v[228:229], v[76:77] neg_lo:[0,0,1] neg_hi:[0,0,1]
	v_pk_fma_f32 v[78:79], v[70:71], v[230:231], v[78:79] neg_lo:[0,0,1] neg_hi:[0,0,1]
	v_cndmask_b32_e64 v67, v67, v75, s[0:1]
	v_cndmask_b32_e64 v66, v66, v74, s[0:1]
	v_cndmask_b32_e64 v65, v65, v73, s[0:1]
	v_cndmask_b32_e64 v64, v64, v72, s[0:1]
	v_cndmask_b32_e64 v71, v71, v79, s[0:1]
	v_cndmask_b32_e64 v70, v70, v78, s[0:1]
	v_cndmask_b32_e64 v69, v69, v77, s[0:1]
	v_cndmask_b32_e64 v68, v68, v76, s[0:1]
	v_pk_mul_f32 v[72:73], v[110:111], v[66:67]
	v_pk_mul_f32 v[66:67], v[204:205], v[64:65]
	v_pk_mul_f32 v[70:71], v[110:111], v[70:71]
	v_pk_mul_f32 v[68:69], v[204:205], v[68:69]
	v_mov_b32_e32 v74, 0
	v_cvt_pk_bf16_f32 v64, v68, v69
	v_cvt_pk_bf16_f32 v65, v70, v71
	v_cvt_pk_bf16_f32 v66, v66, v67
	v_cvt_pk_bf16_f32 v67, v72, v73
	global_store_dwordx4 v[80:81], v[64:67], off offset:256
	v_mov_b32_e32 v68, 0
	v_mov_b32_e32 v72, 0
	v_mov_b32_e32 v65, 0x400
	v_mov_b32_e32 v64, 1.0
	v_lshl_add_u32 v80, v184, 3, v65
	v_mov_b32_e32 v73, 0
	v_mov_b32_e32 v75, 0
	v_mov_b32_e32 v76, 1.0
	v_mov_b32_e32 v77, 1.0
	v_mov_b32_e32 v78, 1.0
	v_mov_b32_e32 v79, 1.0
	s_and_saveexec_b64 s[4:5], s[0:1]
	s_cbranch_execz .LBB0_745
	v_and_b32_e32 v65, 0x3e78, v80
	v_lshlrev_b32_e32 v160, 2, v65
	v_lshl_add_u64 v[66:67], v[168:169], 0, v[160:161]
	v_lshl_add_u64 v[70:71], v[170:171], 0, v[160:161]
	global_load_dwordx4 v[76:79], v[66:67], off
	global_load_dwordx4 v[72:75], v[70:71], off

; #define EFENCE() asm volatile("" ::: "memory")
;     __device__ __forceinline__ bool operator()(f32x4 (&acc)[2][2][4][2], const pg8::Unit& u, int wr, int wc, int fr, int fq) const {
;     ...
;                 for (int q = 0; q < 2; ++q) { c4[q] = (f32x4){1.f, 1.f, 1.f, 1.f}; s4[q] = (f32x4){0.f, 0.f, 0.f, 0.f};
;                     if (rot) { const int t = (row0 + ai * 128 + (2 * mh + q) * 16) & (SEQ - 1); c4[q] = *(const f32x4*)(cosT + t * 8 + 4 * fq); s4[q] = *(const f32x4*)(sinT + t * 8 + 4 * fq); } }
; #pragma unroll
;                 for (int q = 0; q < 2; ++q) { const int m = 2 * mh + q; const int row = row0 + ai * 128 + m * 16; const float rsv = RS_AT(ai, m);
; #pragma unroll
;                     for (int bj = 0; bj < 2; ++bj) { f32x4 x1 = acc[ai][bj][m][0] * rsv, x2 = acc[ai][bj][m][1] * rsv;
;                         const f32x4 y1 = x1 * c4[q] - x2 * s4[q], y2 = x2 * c4[q] + x1 * s4[q];
;                         if (rot) { x1 = y1; x2 = y2; }
;                         st8(dst + (size_t)row * DM + colb + bj * 128, x1 * sc, x2 * sc); } }
;                 EFENCE(); }
.LBB0_747:
	s_or_b64 exec, exec, s[4:5]
	v_mov_b32_e32 v220, 1.0
	v_mov_b32_e32 v221, 1.0
	v_mov_b32_e32 v222, 1.0
	v_mov_b32_e32 v223, 1.0
	v_mov_b32_e32 v224, 0
	v_mov_b32_e32 v225, 0
	v_mov_b32_e32 v226, 0
	v_mov_b32_e32 v227, 0
	v_mov_b32_e32 v228, 1.0
	v_mov_b32_e32 v229, 1.0
	v_mov_b32_e32 v230, 1.0
	v_mov_b32_e32 v231, 1.0
	v_mov_b32_e32 v232, 0
	v_mov_b32_e32 v233, 0
	v_mov_b32_e32 v234, 0
	v_mov_b32_e32 v235, 0
	s_and_saveexec_b64 s[4:5], s[0:1]
	s_cbranch_execz .Lrot_749
	v_and_b32_e32 v218, 0x3e78, v80
	v_lshlrev_b32_e32 v160, 2, v218
	v_lshl_add_u64 v[218:219], v[168:169], 0, v[160:161]
	global_load_dwordx4 v[220:223], v[218:219], off offset:1024
	global_load_dwordx4 v[228:231], v[218:219], off offset:1536
	v_lshl_add_u64 v[218:219], v[170:171], 0, v[160:161]
	global_load_dwordx4 v[224:227], v[218:219], off offset:1024
	global_load_dwordx4 v[232:235], v[218:219], off offset:1536
.Lrot_749:
	s_or_b64 exec, exec, s[4:5]
	v_pk_mul_f32 v[58:59], v[58:59], v[152:153] op_sel_hi:[1,0]
	v_pk_mul_f32 v[56:57], v[56:57], v[152:153] op_sel_hi:[1,0]
	v_pk_mul_f32 v[62:63], v[62:63], v[152:153] op_sel_hi:[1,0]
	v_pk_mul_f32 v[60:61], v[60:61], v[152:153] op_sel_hi:[1,0]
	s_waitcnt vmcnt(5)
	v_pk_mul_f32 v[84:85], v[58:59], v[78:79]
	v_pk_mul_f32 v[86:87], v[56:57], v[76:77]
	s_waitcnt vmcnt(0)
	v_pk_fma_f32 v[84:85], v[62:63], v[74:75], v[84:85]
	v_pk_fma_f32 v[86:87], v[60:61], v[72:73], v[86:87]
	v_pk_mul_f32 v[88:89], v[58:59], v[74:75]
	v_pk_mul_f32 v[90:91], v[56:57], v[72:73]
	v_pk_fma_f32 v[88:89], v[62:63], v[78:79], v[88:89] neg_lo:[0,0,1] neg_hi:[0,0,1]
	v_pk_fma_f32 v[90:91], v[60:61], v[76:77], v[90:91] neg_lo:[0,0,1] neg_hi:[0,0,1]
	v_cndmask_b32_e64 v59, v59, v85, s[0:1]
	v_cndmask_b32_e64 v58, v58, v84, s[0:1]
	v_cndmask_b32_e64 v57, v57, v87, s[0:1]
	v_cndmask_b32_e64 v56, v56, v86, s[0:1]
	v_mov_b32_e32 v84, v204
	v_mov_b32_e32 v85, v204
	v_lshlrev_b64 v[82:83], 11, v[182:183]
	v_cndmask_b32_e64 v63, v63, v89, s[0:1]
	v_cndmask_b32_e64 v62, v62, v88, s[0:1]
	v_cndmask_b32_e64 v61, v61, v91, s[0:1]
	v_cndmask_b32_e64 v60, v60, v90, s[0:1]
	v_pk_mul_f32 v[86:87], v[84:85], v[58:59]
	v_pk_mul_f32 v[58:59], v[204:205], v[56:57]
	v_lshl_add_u64 v[82:83], v[206:207], 0, v[82:83]
	v_pk_mul_f32 v[62:63], v[84:85], v[62:63]
	v_pk_mul_f32 v[60:61], v[204:205], v[60:61]
	v_pk_mul_f32 v[50:51], v[50:51], v[152:153] op_sel_hi:[1,0]
	v_cvt_pk_bf16_f32 v56, v60, v61
	v_cvt_pk_bf16_f32 v57, v62, v63
	v_cvt_pk_bf16_f32 v58, v58, v59
	v_cvt_pk_bf16_f32 v59, v86, v87
	v_pk_mul_f32 v[48:49], v[48:49], v[152:153] op_sel_hi:[1,0]
	global_store_dwordx4 v[82:83], v[56:59], off
	v_pk_mul_f32 v[54:55], v[54:55], v[152:153] op_sel_hi:[1,0]
	v_pk_mul_f32 v[52:53], v[52:53], v[152:153] op_sel_hi:[1,0]
	v_pk_mul_f32 v[56:57], v[50:51], v[78:79]
	v_pk_mul_f32 v[58:59], v[48:49], v[76:77]
	v_pk_fma_f32 v[56:57], v[54:55], v[74:75], v[56:57]
	v_pk_fma_f32 v[58:59], v[52:53], v[72:73], v[58:59]
	v_pk_mul_f32 v[60:61], v[50:51], v[74:75]
	v_pk_mul_f32 v[62:63], v[48:49], v[72:73]
	v_pk_fma_f32 v[60:61], v[54:55], v[78:79], v[60:61] neg_lo:[0,0,1] neg_hi:[0,0,1]
	v_pk_fma_f32 v[62:63], v[52:53], v[76:77], v[62:63] neg_lo:[0,0,1] neg_hi:[0,0,1]
	v_cndmask_b32_e64 v51, v51, v57, s[0:1]
	v_cndmask_b32_e64 v50, v50, v56, s[0:1]
	v_cndmask_b32_e64 v49, v49, v59, s[0:1]
	v_cndmask_b32_e64 v48, v48, v58, s[0:1]
	v_cndmask_b32_e64 v55, v55, v61, s[0:1]
	v_cndmask_b32_e64 v54, v54, v60, s[0:1]
	v_cndmask_b32_e64 v53, v53, v63, s[0:1]
	v_cndmask_b32_e64 v52, v52, v62, s[0:1]
	v_pk_mul_f32 v[56:57], v[84:85], v[50:51]
	v_pk_mul_f32 v[50:51], v[204:205], v[48:49]
	v_pk_mul_f32 v[54:55], v[84:85], v[54:55]
	v_pk_mul_f32 v[52:53], v[204:205], v[52:53]
	v_pk_mul_f32 v[42:43], v[42:43], v[150:151] op_sel_hi:[1,0]
	v_cvt_pk_bf16_f32 v48, v52, v53
	v_cvt_pk_bf16_f32 v49, v54, v55
	v_cvt_pk_bf16_f32 v50, v50, v51
	v_cvt_pk_bf16_f32 v51, v56, v57
	v_pk_mul_f32 v[40:41], v[40:41], v[150:151] op_sel_hi:[1,0]
	global_store_dwordx4 v[82:83], v[48:51], off offset:256
	v_pk_mul_f32 v[46:47], v[46:47], v[150:151] op_sel_hi:[1,0]
	v_pk_mul_f32 v[44:45], v[44:45], v[150:151] op_sel_hi:[1,0]
	v_pk_mul_f32 v[50:51], v[40:41], v[64:65]
	v_pk_mul_f32 v[52:53], v[42:43], v[66:67]
	v_pk_fma_f32 v[50:51], v[44:45], v[68:69], v[50:51]
	v_pk_fma_f32 v[52:53], v[46:47], v[70:71], v[52:53]
	v_pk_mul_f32 v[54:55], v[40:41], v[68:69]
	v_pk_mul_f32 v[56:57], v[42:43], v[70:71]
	v_pk_fma_f32 v[54:55], v[44:45], v[64:65], v[54:55] neg_lo:[0,0,1] neg_hi:[0,0,1]
	v_pk_fma_f32 v[56:57], v[46:47], v[66:67], v[56:57] neg_lo:[0,0,1] neg_hi:[0,0,1]
	v_cndmask_b32_e64 v43, v43, v53, s[0:1]
	v_cndmask_b32_e64 v42, v42, v52, s[0:1]
	v_cndmask_b32_e64 v41, v41, v51, s[0:1]
	v_cndmask_b32_e64 v40, v40, v50, s[0:1]
	v_lshlrev_b64 v[48:49], 11, v[180:181]
	v_cndmask_b32_e64 v47, v47, v57, s[0:1]
	v_cndmask_b32_e64 v46, v46, v56, s[0:1]
	v_cndmask_b32_e64 v45, v45, v55, s[0:1]
	v_cndmask_b32_e64 v44, v44, v54, s[0:1]
	v_pk_mul_f32 v[50:51], v[84:85], v[42:43]
	v_pk_mul_f32 v[42:43], v[204:205], v[40:41]
	v_lshl_add_u64 v[48:49], v[206:207], 0, v[48:49]
	v_pk_mul_f32 v[46:47], v[84:85], v[46:47]
	v_pk_mul_f32 v[44:45], v[204:205], v[44:45]
	v_pk_mul_f32 v[34:35], v[34:35], v[150:151] op_sel_hi:[1,0]
	v_cvt_pk_bf16_f32 v40, v44, v45
	v_cvt_pk_bf16_f32 v41, v46, v47
	v_cvt_pk_bf16_f32 v42, v42, v43
	v_cvt_pk_bf16_f32 v43, v50, v51
	v_pk_mul_f32 v[32:33], v[32:33], v[150:151] op_sel_hi:[1,0]
	global_store_dwordx4 v[48:49], v[40:43], off
	v_pk_mul_f32 v[38:39], v[38:39], v[150:151] op_sel_hi:[1,0]
	v_pk_mul_f32 v[36:37], v[36:37], v[150:151] op_sel_hi:[1,0]
	v_pk_mul_f32 v[40:41], v[32:33], v[64:65]
; #define EFENCE() asm volatile("" ::: "memory")
;     __device__ __forceinline__ bool operator()(f32x4 (&acc)[2][2][4][2], const pg8::Unit& u, int wr, int wc, int fr, int fq) const {
;     ...
;                 for (int q = 0; q < 2; ++q) { c4[q] = (f32x4){1.f, 1.f, 1.f, 1.f}; s4[q] = (f32x4){0.f, 0.f, 0.f, 0.f};
;                     if (rot) { const int t = (row0 + ai * 128 + (2 * mh + q) * 16) & (SEQ - 1); c4[q] = *(const f32x4*)(cosT + t * 8 + 4 * fq); s4[q] = *(const f32x4*)(sinT + t * 8 + 4 * fq); } }
; #pragma unroll
;                 for (int q = 0; q < 2; ++q) { const int m = 2 * mh + q; const int row = row0 + ai * 128 + m * 16; const float rsv = RS_AT(ai, m);
; #pragma unroll
;                     for (int bj = 0; bj < 2; ++bj) { f32x4 x1 = acc[ai][bj][m][0] * rsv, x2 = acc[ai][bj][m][1] * rsv;
;                         const f32x4 y1 = x1 * c4[q] - x2 * s4[q], y2 = x2 * c4[q] + x1 * s4[q];
;                         if (rot) { x1 = y1; x2 = y2; }
;                         st8(dst + (size_t)row * DM + colb + bj * 128, x1 * sc, x2 * sc); } }
;                 EFENCE(); }
	v_pk_mul_f32 v[42:43], v[34:35], v[66:67]
	v_pk_fma_f32 v[40:41], v[36:37], v[68:69], v[40:41]
	v_pk_fma_f32 v[42:43], v[38:39], v[70:71], v[42:43]
	v_pk_mul_f32 v[44:45], v[32:33], v[68:69]
	v_pk_mul_f32 v[46:47], v[34:35], v[70:71]
	v_pk_fma_f32 v[44:45], v[36:37], v[64:65], v[44:45] neg_lo:[0,0,1] neg_hi:[0,0,1]
	v_pk_fma_f32 v[46:47], v[38:39], v[66:67], v[46:47] neg_lo:[0,0,1] neg_hi:[0,0,1]
	v_cndmask_b32_e64 v35, v35, v43, s[0:1]
	v_cndmask_b32_e64 v34, v34, v42, s[0:1]
	v_cndmask_b32_e64 v33, v33, v41, s[0:1]
	v_cndmask_b32_e64 v32, v32, v40, s[0:1]
	v_cndmask_b32_e64 v39, v39, v47, s[0:1]
	v_cndmask_b32_e64 v38, v38, v46, s[0:1]
	v_cndmask_b32_e64 v37, v37, v45, s[0:1]
	v_cndmask_b32_e64 v36, v36, v44, s[0:1]
	v_pk_mul_f32 v[40:41], v[84:85], v[34:35]
	v_pk_mul_f32 v[34:35], v[204:205], v[32:33]
	v_pk_mul_f32 v[38:39], v[84:85], v[38:39]
	v_pk_mul_f32 v[36:37], v[204:205], v[36:37]
	v_mov_b32_e32 v42, 0
	v_cvt_pk_bf16_f32 v32, v36, v37
	v_cvt_pk_bf16_f32 v33, v38, v39
	v_cvt_pk_bf16_f32 v34, v34, v35
	v_cvt_pk_bf16_f32 v35, v40, v41
	global_store_dwordx4 v[48:49], v[32:35], off offset:256
	v_pk_mul_f32 v[26:27], v[26:27], v[148:149] op_sel_hi:[1,0]
	v_pk_mul_f32 v[24:25], v[24:25], v[148:149] op_sel_hi:[1,0]
	v_pk_mul_f32 v[30:31], v[30:31], v[148:149] op_sel_hi:[1,0]
	v_pk_mul_f32 v[28:29], v[28:29], v[148:149] op_sel_hi:[1,0]
	v_pk_mul_f32 v[50:51], v[26:27], v[222:223]
	v_pk_mul_f32 v[52:53], v[24:25], v[220:221]
	v_pk_fma_f32 v[50:51], v[30:31], v[226:227], v[50:51]
	v_pk_fma_f32 v[52:53], v[28:29], v[224:225], v[52:53]
	v_pk_mul_f32 v[54:55], v[26:27], v[226:227]
	v_pk_mul_f32 v[56:57], v[24:25], v[224:225]
	v_pk_fma_f32 v[54:55], v[30:31], v[222:223], v[54:55] neg_lo:[0,0,1] neg_hi:[0,0,1]
	v_pk_fma_f32 v[56:57], v[28:29], v[220:221], v[56:57] neg_lo:[0,0,1] neg_hi:[0,0,1]
	v_cndmask_b32_e64 v27, v27, v51, s[0:1]
	v_cndmask_b32_e64 v26, v26, v50, s[0:1]
	v_cndmask_b32_e64 v25, v25, v53, s[0:1]
	v_cndmask_b32_e64 v24, v24, v52, s[0:1]
	v_mov_b32_e32 v50, v204
	v_mov_b32_e32 v51, v204
	v_lshlrev_b64 v[48:49], 11, v[178:179]
	v_cndmask_b32_e64 v31, v31, v55, s[0:1]
	v_cndmask_b32_e64 v30, v30, v54, s[0:1]
	v_cndmask_b32_e64 v29, v29, v57, s[0:1]
	v_cndmask_b32_e64 v28, v28, v56, s[0:1]
	v_pk_mul_f32 v[52:53], v[50:51], v[26:27]
	v_pk_mul_f32 v[26:27], v[204:205], v[24:25]
	v_lshl_add_u64 v[48:49], v[206:207], 0, v[48:49]
	v_pk_mul_f32 v[30:31], v[50:51], v[30:31]
	v_pk_mul_f32 v[28:29], v[204:205], v[28:29]
	v_pk_mul_f32 v[18:19], v[18:19], v[148:149] op_sel_hi:[1,0]
	v_cvt_pk_bf16_f32 v24, v28, v29
	v_cvt_pk_bf16_f32 v25, v30, v31
	v_cvt_pk_bf16_f32 v26, v26, v27
	v_cvt_pk_bf16_f32 v27, v52, v53
	v_pk_mul_f32 v[16:17], v[16:17], v[148:149] op_sel_hi:[1,0]
	global_store_dwordx4 v[48:49], v[24:27], off
	v_pk_mul_f32 v[22:23], v[22:23], v[148:149] op_sel_hi:[1,0]
	v_pk_mul_f32 v[20:21], v[20:21], v[148:149] op_sel_hi:[1,0]
	v_pk_mul_f32 v[24:25], v[18:19], v[222:223]
	v_pk_mul_f32 v[26:27], v[16:17], v[220:221]
	v_pk_fma_f32 v[24:25], v[22:23], v[226:227], v[24:25]
	v_pk_fma_f32 v[26:27], v[20:21], v[224:225], v[26:27]
	v_pk_mul_f32 v[28:29], v[18:19], v[226:227]
	v_pk_mul_f32 v[30:31], v[16:17], v[224:225]
	v_pk_fma_f32 v[28:29], v[22:23], v[222:223], v[28:29] neg_lo:[0,0,1] neg_hi:[0,0,1]
	v_pk_fma_f32 v[30:31], v[20:21], v[220:221], v[30:31] neg_lo:[0,0,1] neg_hi:[0,0,1]
	v_cndmask_b32_e64 v19, v19, v25, s[0:1]
	v_cndmask_b32_e64 v18, v18, v24, s[0:1]
	v_cndmask_b32_e64 v17, v17, v27, s[0:1]
	v_cndmask_b32_e64 v16, v16, v26, s[0:1]
	v_cndmask_b32_e64 v23, v23, v29, s[0:1]
	v_cndmask_b32_e64 v22, v22, v28, s[0:1]
	v_cndmask_b32_e64 v21, v21, v31, s[0:1]
	v_cndmask_b32_e64 v20, v20, v30, s[0:1]
	v_pk_mul_f32 v[24:25], v[50:51], v[18:19]
	v_pk_mul_f32 v[18:19], v[204:205], v[16:17]
	v_pk_mul_f32 v[22:23], v[50:51], v[22:23]
	v_pk_mul_f32 v[20:21], v[204:205], v[20:21]
	v_pk_mul_f32 v[10:11], v[10:11], v[146:147] op_sel_hi:[1,0]
	v_cvt_pk_bf16_f32 v16, v20, v21
	v_cvt_pk_bf16_f32 v17, v22, v23
	v_cvt_pk_bf16_f32 v18, v18, v19
	v_cvt_pk_bf16_f32 v19, v24, v25
	v_pk_mul_f32 v[8:9], v[8:9], v[146:147] op_sel_hi:[1,0]
	global_store_dwordx4 v[48:49], v[16:19], off offset:256
	v_pk_mul_f32 v[14:15], v[14:15], v[146:147] op_sel_hi:[1,0]
	v_pk_mul_f32 v[12:13], v[12:13], v[146:147] op_sel_hi:[1,0]
	v_pk_mul_f32 v[18:19], v[8:9], v[228:229]
	v_pk_mul_f32 v[20:21], v[10:11], v[230:231]
	v_pk_fma_f32 v[18:19], v[12:13], v[232:233], v[18:19]
	v_pk_fma_f32 v[20:21], v[14:15], v[234:235], v[20:21]
	v_pk_mul_f32 v[22:23], v[8:9], v[232:233]
	v_pk_mul_f32 v[24:25], v[10:11], v[234:235]
	v_pk_fma_f32 v[22:23], v[12:13], v[228:229], v[22:23] neg_lo:[0,0,1] neg_hi:[0,0,1]
	v_pk_fma_f32 v[24:25], v[14:15], v[230:231], v[24:25] neg_lo:[0,0,1] neg_hi:[0,0,1]
	v_cndmask_b32_e64 v11, v11, v21, s[0:1]
	v_cndmask_b32_e64 v10, v10, v20, s[0:1]
	v_cndmask_b32_e64 v9, v9, v19, s[0:1]
	v_cndmask_b32_e64 v8, v8, v18, s[0:1]
	v_lshlrev_b64 v[16:17], 11, v[176:177]
	v_cndmask_b32_e64 v15, v15, v25, s[0:1]
	v_cndmask_b32_e64 v14, v14, v24, s[0:1]
	v_cndmask_b32_e64 v13, v13, v23, s[0:1]
	v_cndmask_b32_e64 v12, v12, v22, s[0:1]
	v_pk_mul_f32 v[18:19], v[50:51], v[10:11]
	v_pk_mul_f32 v[10:11], v[204:205], v[8:9]
	v_lshl_add_u64 v[16:17], v[206:207], 0, v[16:17]
	v_pk_mul_f32 v[14:15], v[50:51], v[14:15]
	v_pk_mul_f32 v[12:13], v[204:205], v[12:13]
	v_pk_mul_f32 v[2:3], v[2:3], v[146:147] op_sel_hi:[1,0]
	v_cvt_pk_bf16_f32 v8, v12, v13
	v_cvt_pk_bf16_f32 v9, v14, v15
	v_cvt_pk_bf16_f32 v10, v10, v11
	v_cvt_pk_bf16_f32 v11, v18, v19
	v_pk_mul_f32 v[0:1], v[0:1], v[146:147] op_sel_hi:[1,0]
	global_store_dwordx4 v[16:17], v[8:11], off
	v_pk_mul_f32 v[6:7], v[6:7], v[146:147] op_sel_hi:[1,0]
	v_pk_mul_f32 v[4:5], v[4:5], v[146:147] op_sel_hi:[1,0]
	v_pk_mul_f32 v[8:9], v[0:1], v[228:229]
	v_pk_mul_f32 v[10:11], v[2:3], v[230:231]
	v_pk_fma_f32 v[8:9], v[4:5], v[232:233], v[8:9]
	v_pk_fma_f32 v[10:11], v[6:7], v[234:235], v[10:11]
	v_pk_mul_f32 v[12:13], v[0:1], v[232:233]
	v_pk_mul_f32 v[14:15], v[2:3], v[234:235]
	v_pk_fma_f32 v[12:13], v[4:5], v[228:229], v[12:13] neg_lo:[0,0,1] neg_hi:[0,0,1]
	v_pk_fma_f32 v[14:15], v[6:7], v[230:231], v[14:15] neg_lo:[0,0,1] neg_hi:[0,0,1]
	v_cndmask_b32_e64 v3, v3, v11, s[0:1]
	v_cndmask_b32_e64 v2, v2, v10, s[0:1]
	v_cndmask_b32_e64 v1, v1, v9, s[0:1]
	v_cndmask_b32_e64 v0, v0, v8, s[0:1]
	v_cndmask_b32_e64 v7, v7, v15, s[0:1]
	v_cndmask_b32_e64 v6, v6, v14, s[0:1]
	v_cndmask_b32_e64 v5, v5, v13, s[0:1]
	v_cndmask_b32_e64 v4, v4, v12, s[0:1]
	v_pk_mul_f32 v[8:9], v[50:51], v[2:3]
	v_pk_mul_f32 v[2:3], v[204:205], v[0:1]
	v_pk_mul_f32 v[6:7], v[50:51], v[6:7]
	v_pk_mul_f32 v[4:5], v[204:205], v[4:5]
	s_nop 0
	v_cvt_pk_bf16_f32 v0, v4, v5
	v_cvt_pk_bf16_f32 v1, v6, v7
	v_cvt_pk_bf16_f32 v2, v2, v3
	v_cvt_pk_bf16_f32 v3, v8, v9
	global_store_dwordx4 v[16:17], v[0:3], off offset:256
	s_andn2_b64 vcc, exec, s[6:7]
	s_mov_b64 s[4:5], -1
	s_cbranch_vccnz .LBB0_712
